# static s_setprio 1 for waves 4-7 during attention items (reset at item end)
# baseline (speedup 1.0000x reference)
.Lc3_attn:
	s_lshr_b32 s101, s93, 6
	s_cmp_ge_u32 s101, 4
	s_cbranch_scc0 .Lprio_skip
	s_setprio 1

.LBB0_869:
	s_setprio 0
	s_and_saveexec_b64 s[2:3], s[36:37]
	s_cbranch_execz .LBB0_791
	v_readlane_b32 s12, v253, 54
	s_nop 1
	v_mov_b32_e32 v0, s12
	s_waitcnt vmcnt(0)
	ds_write_b32 v0, v196
	s_branch .LBB0_791
